# adds phase 0: once-read f32 weight / x loads use the nt cache policy
# baseline (speedup 1.0000x reference)
.LBB0_34:
.LBB0_35:
	s_ashr_i32 s7, s6, 31
	v_lshlrev_b32_e32 v2, 2, v136
	s_lshl_b64 s[10:11], s[6:7], 2
	v_lshrrev_b32_e32 v141, 4, v136
	v_and_b32_e32 v68, 60, v2
	s_add_u32 s10, s0, s10
	v_or_b32_e32 v62, s8, v141
	s_addc_u32 s11, s1, s11
	v_mov_b32_e32 v133, 0
	v_lshlrev_b32_e32 v132, 2, v68
	v_lshl_add_u64 v[58:59], s[10:11], 0, v[132:133]
	s_ashr_i32 s7, s8, 31
	v_mad_u64_u32 v[2:3], s[10:11], v62, s61, 0
	v_or_b32_e32 v4, 4, v62
	v_or_b32_e32 v10, 8, v62
	v_or_b32_e32 v12, 12, v62
	v_or_b32_e32 v18, 16, v62
	v_or_b32_e32 v20, 20, v62
	v_or_b32_e32 v26, 24, v62
	v_or_b32_e32 v28, 28, v62
	v_or_b32_e32 v34, 32, v62
	v_or_b32_e32 v36, 36, v62
	v_or_b32_e32 v42, 40, v62
	v_or_b32_e32 v44, 44, v62
	v_or_b32_e32 v50, 48, v62
	v_or_b32_e32 v52, 52, v62
	v_or_b32_e32 v60, 56, v62
	v_or_b32_e32 v62, 60, v62
	s_mul_i32 s7, s7, s61
	v_mad_u64_u32 v[4:5], s[10:11], v4, s61, 0
	v_mad_u64_u32 v[10:11], s[10:11], v10, s61, 0
	v_mad_u64_u32 v[12:13], s[10:11], v12, s61, 0
	v_mad_u64_u32 v[18:19], s[10:11], v18, s61, 0
	v_mad_u64_u32 v[20:21], s[10:11], v20, s61, 0
	v_mad_u64_u32 v[26:27], s[10:11], v26, s61, 0
	v_mad_u64_u32 v[28:29], s[10:11], v28, s61, 0
	v_mad_u64_u32 v[34:35], s[10:11], v34, s61, 0
	v_mad_u64_u32 v[36:37], s[10:11], v36, s61, 0
	v_mad_u64_u32 v[42:43], s[10:11], v42, s61, 0
	v_mad_u64_u32 v[44:45], s[10:11], v44, s61, 0
	v_mad_u64_u32 v[50:51], s[10:11], v50, s61, 0
	v_mad_u64_u32 v[52:53], s[10:11], v52, s61, 0
	v_mad_u64_u32 v[60:61], s[10:11], v60, s61, 0
	v_mad_u64_u32 v[62:63], s[10:11], v62, s61, 0
	v_add_u32_e32 v3, s7, v3
	v_add_u32_e32 v5, s7, v5
	v_add_u32_e32 v11, s7, v11
	v_add_u32_e32 v13, s7, v13
	v_add_u32_e32 v19, s7, v19
	v_add_u32_e32 v21, s7, v21
	v_add_u32_e32 v27, s7, v27
	v_add_u32_e32 v29, s7, v29
	v_add_u32_e32 v35, s7, v35
	v_add_u32_e32 v37, s7, v37
	v_add_u32_e32 v43, s7, v43
	v_add_u32_e32 v45, s7, v45
	v_add_u32_e32 v51, s7, v51
	v_add_u32_e32 v53, s7, v53
	v_add_u32_e32 v61, s7, v61
	v_add_u32_e32 v63, s7, v63
	v_lshl_add_u64 v[2:3], v[2:3], 2, v[58:59]
	v_lshl_add_u64 v[4:5], v[4:5], 2, v[58:59]
	v_lshl_add_u64 v[10:11], v[10:11], 2, v[58:59]
	v_lshl_add_u64 v[12:13], v[12:13], 2, v[58:59]
	v_lshl_add_u64 v[18:19], v[18:19], 2, v[58:59]
	v_lshl_add_u64 v[20:21], v[20:21], 2, v[58:59]
	v_lshl_add_u64 v[26:27], v[26:27], 2, v[58:59]
	v_lshl_add_u64 v[28:29], v[28:29], 2, v[58:59]
	v_lshl_add_u64 v[34:35], v[34:35], 2, v[58:59]
	v_lshl_add_u64 v[36:37], v[36:37], 2, v[58:59]
	v_lshl_add_u64 v[42:43], v[42:43], 2, v[58:59]
	v_lshl_add_u64 v[44:45], v[44:45], 2, v[58:59]
	v_lshl_add_u64 v[50:51], v[50:51], 2, v[58:59]
	v_lshl_add_u64 v[52:53], v[52:53], 2, v[58:59]
	v_lshl_add_u64 v[60:61], v[60:61], 2, v[58:59]
	v_lshl_add_u64 v[58:59], v[62:63], 2, v[58:59]
	global_load_dwordx4 v[6:9], v[2:3], off nt
	s_nop 0
	global_load_dwordx4 v[2:5], v[4:5], off nt
	s_nop 0
	global_load_dwordx4 v[14:17], v[10:11], off nt
	s_nop 0
	global_load_dwordx4 v[10:13], v[12:13], off nt
	s_nop 0
	global_load_dwordx4 v[22:25], v[18:19], off nt
	s_nop 0
	global_load_dwordx4 v[18:21], v[20:21], off nt
	s_nop 0
	global_load_dwordx4 v[30:33], v[26:27], off nt
	s_nop 0
	global_load_dwordx4 v[26:29], v[28:29], off nt
	s_nop 0
	global_load_dwordx4 v[38:41], v[34:35], off nt
	s_nop 0
	global_load_dwordx4 v[34:37], v[36:37], off nt
	s_nop 0
	global_load_dwordx4 v[46:49], v[42:43], off nt
	s_nop 0
	global_load_dwordx4 v[42:45], v[44:45], off nt
	s_nop 0
	global_load_dwordx4 v[54:57], v[50:51], off nt
	s_nop 0
	global_load_dwordx4 v[50:53], v[52:53], off nt
	s_nop 0
	global_load_dwordx4 v[62:65], v[60:61], off nt
	s_nop 0
	global_load_dwordx4 v[58:61], v[58:59], off nt
	v_and_b32_e32 v130, 56, v66
	v_mul_u32_u24_e32 v66, 0x104, v130
	v_lshlrev_b32_e32 v70, 2, v140
	v_add3_u32 v143, s41, v66, v70
	v_lshrrev_b32_e32 v66, 2, v136
	v_or_b32_e32 v137, 8, v140
	v_and_b32_e32 v144, 8, v66
	v_lshlrev_b32_e32 v66, 1, v137
	v_or_b32_e32 v139, 24, v140
	v_and_b32_e32 v145, 24, v66
	v_lshlrev_b32_e32 v66, 1, v139
	v_or_b32_e32 v148, 40, v140
	v_writelane_b32 v239, s39, 46
	v_and_b32_e32 v146, 56, v66
	v_lshlrev_b32_e32 v66, 1, v148
	v_or_b32_e32 v151, 56, v140
	v_add_u32_e32 v67, s41, v132
	v_mul_u32_u24_e32 v69, 0x104, v141
	v_writelane_b32 v239, s41, 48
	v_and_b32_e32 v149, 0x58, v66
	v_lshlrev_b32_e32 v66, 1, v151
	s_mov_b32 s12, s52
	v_mov_b32_e32 v131, v133
	v_bfe_u32 v142, v136, 3, 2
	v_or_b32_e32 v138, 16, v140
	v_or_b32_e32 v147, 32, v140
	v_or_b32_e32 v150, 48, v140
	v_and_b32_e32 v152, 0x78, v66
	s_add_i32 s7, s94, 0xffffd100
	v_lshlrev_b32_e32 v134, 2, v68
	v_add_u32_e32 v153, v67, v69
	v_lshlrev_b32_e32 v132, 1, v130
	s_mov_b32 s63, s60
	s_mov_b32 s80, s91
	s_mov_b32 s81, s92
	s_mov_b64 s[10:11], s[4:5]
	v_writelane_b32 v239, s12, 49
	s_mov_b32 s93, s44
	s_nop 0
	v_writelane_b32 v239, s13, 50
	s_branch .LBB0_37

.LBB0_60:
	s_waitcnt vmcnt(15)
	v_mov_b64_e32 v[68:69], v[8:9]
	s_waitcnt vmcnt(14)
	v_mov_b64_e32 v[72:73], v[4:5]
	s_waitcnt vmcnt(13)
	v_mov_b64_e32 v[76:77], v[16:17]
	s_waitcnt vmcnt(12)
	v_mov_b64_e32 v[80:81], v[12:13]
	s_waitcnt vmcnt(11)
	v_mov_b64_e32 v[84:85], v[24:25]
	s_waitcnt vmcnt(10)
	v_mov_b64_e32 v[88:89], v[20:21]
	s_waitcnt vmcnt(9)
	v_mov_b64_e32 v[92:93], v[32:33]
	s_waitcnt vmcnt(8)
	v_mov_b64_e32 v[96:97], v[28:29]
	s_waitcnt vmcnt(7)
	v_mov_b64_e32 v[100:101], v[40:41]
	s_waitcnt vmcnt(6)
	v_mov_b64_e32 v[104:105], v[36:37]
	s_waitcnt vmcnt(5)
	v_mov_b64_e32 v[108:109], v[48:49]
	s_waitcnt vmcnt(4)
	v_mov_b64_e32 v[112:113], v[44:45]
	s_waitcnt vmcnt(3)
	v_mov_b64_e32 v[116:117], v[56:57]
	s_waitcnt vmcnt(2)
	v_mov_b64_e32 v[120:121], v[52:53]
	s_waitcnt vmcnt(1)
	v_mov_b64_e32 v[124:125], v[64:65]
	s_waitcnt vmcnt(0)
	v_mov_b64_e32 v[128:129], v[60:61]
	s_mov_b64 s[36:37], 0
	s_andn2_b64 vcc, exec, s[38:39]
	v_mov_b64_e32 v[66:67], v[6:7]
	v_mov_b64_e32 v[70:71], v[2:3]
	v_mov_b64_e32 v[74:75], v[14:15]
	v_mov_b64_e32 v[78:79], v[10:11]
	v_mov_b64_e32 v[82:83], v[22:23]
	v_mov_b64_e32 v[86:87], v[18:19]
	v_mov_b64_e32 v[90:91], v[30:31]
	v_mov_b64_e32 v[94:95], v[26:27]
	v_mov_b64_e32 v[98:99], v[38:39]
	v_mov_b64_e32 v[102:103], v[34:35]
	v_mov_b64_e32 v[106:107], v[46:47]
	v_mov_b64_e32 v[110:111], v[42:43]
	v_mov_b64_e32 v[114:115], v[54:55]
	v_mov_b64_e32 v[118:119], v[50:51]
	v_mov_b64_e32 v[122:123], v[62:63]
	v_mov_b64_e32 v[126:127], v[58:59]
	s_cbranch_vccz .LBB0_36
	s_ashr_i32 s35, s34, 31
	s_lshl_b64 s[0:1], s[34:35], 2
	v_add_u32_e32 v128, s83, v141
	s_add_u32 s0, s14, s0
	s_addc_u32 s1, s15, s1
	v_mov_b32_e32 v135, v133
	v_add_u32_e32 v74, 8, v128
	v_add_u32_e32 v82, 16, v128
	v_add_u32_e32 v90, 24, v128
	v_add_u32_e32 v98, 32, v128
	v_add_u32_e32 v106, 40, v128
	v_add_u32_e32 v114, 48, v128
	v_add_u32_e32 v124, 56, v128
	v_lshl_add_u64 v[122:123], s[0:1], 0, v[134:135]
	v_mad_u64_u32 v[66:67], s[0:1], v128, s89, 0
	v_ashrrev_i32_e32 v77, 31, v74
	v_mad_u64_u32 v[74:75], s[0:1], v74, s89, 0
	v_ashrrev_i32_e32 v85, 31, v82
	v_mad_u64_u32 v[82:83], s[0:1], v82, s89, 0
	v_ashrrev_i32_e32 v93, 31, v90
	v_mad_u64_u32 v[90:91], s[0:1], v90, s89, 0
	v_ashrrev_i32_e32 v101, 31, v98
	v_mad_u64_u32 v[98:99], s[0:1], v98, s89, 0
	v_ashrrev_i32_e32 v109, 31, v106
	v_mad_u64_u32 v[106:107], s[0:1], v106, s89, 0
	v_ashrrev_i32_e32 v117, 31, v114
	v_mad_u64_u32 v[114:115], s[0:1], v114, s89, 0
	v_ashrrev_i32_e32 v127, 31, v124
	v_mad_u64_u32 v[124:125], s[0:1], v124, s89, 0
	v_ashrrev_i32_e32 v69, 31, v128
	v_mov_b32_e32 v68, v67
	v_mov_b32_e32 v76, v75
	v_mov_b32_e32 v84, v83
	v_mov_b32_e32 v92, v91
	v_mov_b32_e32 v100, v99
	v_mov_b32_e32 v108, v107
	v_mov_b32_e32 v116, v115
	v_mov_b32_e32 v126, v125
	v_mad_u64_u32 v[68:69], s[0:1], v69, s89, v[68:69]
	v_mad_u64_u32 v[76:77], s[0:1], v77, s89, v[76:77]
	v_mad_u64_u32 v[84:85], s[0:1], v85, s89, v[84:85]
	v_mad_u64_u32 v[92:93], s[0:1], v93, s89, v[92:93]
	v_mad_u64_u32 v[100:101], s[0:1], v101, s89, v[100:101]
	v_mad_u64_u32 v[108:109], s[0:1], v109, s89, v[108:109]
	v_mad_u64_u32 v[116:117], s[0:1], v117, s89, v[116:117]
	v_mad_u64_u32 v[126:127], s[0:1], v127, s89, v[126:127]
	v_mov_b32_e32 v67, v68
	v_add_u32_e32 v68, 4, v128
	v_mov_b32_e32 v75, v76
	v_add_u32_e32 v76, 12, v128
	v_mov_b32_e32 v83, v84
	v_add_u32_e32 v84, 20, v128
	v_mov_b32_e32 v91, v92
	v_add_u32_e32 v92, 28, v128
	v_mov_b32_e32 v99, v100
	v_add_u32_e32 v100, 36, v128
	v_mov_b32_e32 v107, v108
	v_add_u32_e32 v108, 44, v128
	v_mov_b32_e32 v115, v116
	v_add_u32_e32 v116, 52, v128
	v_mov_b32_e32 v125, v126
	v_add_u32_e32 v126, 60, v128
	v_ashrrev_i32_e32 v71, 31, v68
	v_mad_u64_u32 v[68:69], s[0:1], v68, s89, 0
	v_ashrrev_i32_e32 v79, 31, v76
	v_mad_u64_u32 v[76:77], s[0:1], v76, s89, 0
	v_ashrrev_i32_e32 v87, 31, v84
	v_mad_u64_u32 v[84:85], s[0:1], v84, s89, 0
	v_ashrrev_i32_e32 v95, 31, v92
	v_mad_u64_u32 v[92:93], s[0:1], v92, s89, 0
	v_ashrrev_i32_e32 v103, 31, v100
	v_mad_u64_u32 v[100:101], s[0:1], v100, s89, 0
	v_ashrrev_i32_e32 v111, 31, v108
	v_mad_u64_u32 v[108:109], s[0:1], v108, s89, 0
	v_ashrrev_i32_e32 v119, 31, v116
	v_mad_u64_u32 v[116:117], s[0:1], v116, s89, 0
	v_ashrrev_i32_e32 v129, 31, v126
	v_mad_u64_u32 v[126:127], s[0:1], v126, s89, 0
	v_mov_b32_e32 v70, v69
	v_mov_b32_e32 v78, v77
	v_mov_b32_e32 v86, v85
	v_mov_b32_e32 v94, v93
	v_mov_b32_e32 v102, v101
	v_mov_b32_e32 v110, v109
	v_mov_b32_e32 v118, v117
	v_mov_b32_e32 v128, v127
	v_mad_u64_u32 v[70:71], s[0:1], v71, s89, v[70:71]
	v_mad_u64_u32 v[78:79], s[0:1], v79, s89, v[78:79]
	v_mad_u64_u32 v[86:87], s[0:1], v87, s89, v[86:87]
	v_mad_u64_u32 v[94:95], s[0:1], v95, s89, v[94:95]
	v_mad_u64_u32 v[102:103], s[0:1], v103, s89, v[102:103]
	v_mad_u64_u32 v[110:111], s[0:1], v111, s89, v[110:111]
	v_mad_u64_u32 v[118:119], s[0:1], v119, s89, v[118:119]
	v_mad_u64_u32 v[128:129], s[0:1], v129, s89, v[128:129]
	v_mov_b32_e32 v69, v70
	v_mov_b32_e32 v77, v78
	v_mov_b32_e32 v85, v86
	v_mov_b32_e32 v93, v94
	v_mov_b32_e32 v101, v102
	v_mov_b32_e32 v109, v110
	v_mov_b32_e32 v117, v118
	v_mov_b32_e32 v127, v128
	v_lshl_add_u64 v[66:67], v[66:67], 2, v[122:123]
	v_lshl_add_u64 v[70:71], v[68:69], 2, v[122:123]
	v_lshl_add_u64 v[74:75], v[74:75], 2, v[122:123]
	v_lshl_add_u64 v[78:79], v[76:77], 2, v[122:123]
	v_lshl_add_u64 v[82:83], v[82:83], 2, v[122:123]
	v_lshl_add_u64 v[86:87], v[84:85], 2, v[122:123]
	v_lshl_add_u64 v[90:91], v[90:91], 2, v[122:123]
	v_lshl_add_u64 v[94:95], v[92:93], 2, v[122:123]
	v_lshl_add_u64 v[98:99], v[98:99], 2, v[122:123]
	v_lshl_add_u64 v[102:103], v[100:101], 2, v[122:123]
	v_lshl_add_u64 v[106:107], v[106:107], 2, v[122:123]
	v_lshl_add_u64 v[110:111], v[108:109], 2, v[122:123]
	v_lshl_add_u64 v[114:115], v[114:115], 2, v[122:123]
	v_lshl_add_u64 v[118:119], v[116:117], 2, v[122:123]
	v_lshl_add_u64 v[124:125], v[124:125], 2, v[122:123]
	v_lshl_add_u64 v[126:127], v[126:127], 2, v[122:123]
	global_load_dwordx4 v[66:69], v[66:67], off nt
	s_nop 0
	global_load_dwordx4 v[70:73], v[70:71], off nt
	s_nop 0
	global_load_dwordx4 v[74:77], v[74:75], off nt
	s_nop 0
	global_load_dwordx4 v[78:81], v[78:79], off nt
	s_nop 0
	global_load_dwordx4 v[82:85], v[82:83], off nt
	s_nop 0
	global_load_dwordx4 v[86:89], v[86:87], off nt
	s_nop 0
	global_load_dwordx4 v[90:93], v[90:91], off nt
	s_nop 0
	global_load_dwordx4 v[94:97], v[94:95], off nt
	s_nop 0
	global_load_dwordx4 v[98:101], v[98:99], off nt
	s_nop 0
	global_load_dwordx4 v[102:105], v[102:103], off nt
	s_nop 0
	global_load_dwordx4 v[106:109], v[106:107], off nt
	s_nop 0
	global_load_dwordx4 v[110:113], v[110:111], off nt
	s_nop 0
	global_load_dwordx4 v[114:117], v[114:115], off nt
	s_nop 0
	global_load_dwordx4 v[118:121], v[118:119], off nt
	s_nop 0
	global_load_dwordx4 v[122:125], v[124:125], off nt
	s_nop 0
	global_load_dwordx4 v[126:129], v[126:127], off nt
	s_mov_b64 s[36:37], -1
	s_mov_b32 s61, s89
	s_mov_b32 s63, s84
	s_mov_b32 s82, s83
	s_mov_b32 s6, s34
	s_mov_b32 s80, s9
	s_mov_b32 s81, s88
	s_mov_b64 s[10:11], s[12:13]
	s_mov_b64 s[0:1], s[14:15]
	s_branch .LBB0_36

.LBB0_120:
	s_or_b64 exec, exec, s[0:1]
	v_mov_b32_e32 v2, v0
	s_nop 0
	v_ashrrev_i32_e32 v3, 31, v2
	v_lshl_add_u64 v[4:5], v[2:3], 4, s[16:17]
	s_barrier
	global_load_dwordx4 v[4:7], v[4:5], off nt
	v_readfirstlane_b32 s0, v2
	s_ashr_i32 s0, s0, 6
	s_add_i32 s2, s0, s83
	v_lshl_add_u32 v1, v2, 4, 0
	s_cmpk_lt_i32 s2, 0x4000
	s_waitcnt vmcnt(0)
	ds_write_b128 v1, v[4:7]
	s_waitcnt lgkmcnt(0)
	s_barrier
	s_cbranch_scc0 .LBB0_125
	s_ashr_i32 s3, s2, 31
	s_lshl_b64 s[4:5], s[2:3], 13
	v_readlane_b32 s10, v239, 2
	v_and_b32_e32 v38, 63, v2
	v_readlane_b32 s11, v239, 3
	s_add_u32 s4, s10, s4
	s_addc_u32 s5, s11, s5
	v_lshlrev_b32_e32 v34, 4, v38
	v_mov_b32_e32 v35, 0
	v_lshl_add_u64 v[2:3], s[4:5], 0, v[34:35]
	v_add_co_u32_e32 v14, vcc, 0x1000, v2
	v_mbcnt_lo_u32_b32 v36, -1, 0
	s_nop 0
	v_addc_co_u32_e32 v15, vcc, 0, v3, vcc
	global_load_dwordx4 v[18:21], v34, s[4:5] offset:3072
	global_load_dwordx4 v[22:25], v34, s[4:5] offset:2048
	global_load_dwordx4 v[26:29], v34, s[4:5] offset:1024
	global_load_dwordx4 v[2:5], v[14:15], off offset:3072
	global_load_dwordx4 v[6:9], v[14:15], off offset:2048
	global_load_dwordx4 v[10:13], v[14:15], off offset:1024
	s_nop 0
	global_load_dwordx4 v[14:17], v[14:15], off nt
	s_nop 0
	global_load_dwordx4 v[30:33], v34, s[4:5]
	v_mbcnt_hi_u32_b32 v36, -1, v36
	v_and_b32_e32 v37, 64, v36
	v_xor_b32_e32 v39, 1, v36
	v_add_u32_e32 v37, 64, v37
	v_xor_b32_e32 v40, 2, v36
	v_cmp_lt_i32_e32 vcc, v39, v37
	v_xor_b32_e32 v41, 4, v36
	v_xor_b32_e32 v42, 8, v36
	v_cndmask_b32_e32 v39, v36, v39, vcc
	v_cmp_lt_i32_e32 vcc, v40, v37
	s_add_i32 s4, s2, s94
	v_xor_b32_e32 v43, 16, v36
	v_cndmask_b32_e32 v40, v36, v40, vcc
	v_cmp_lt_i32_e32 vcc, v41, v37
	s_ashr_i32 s5, s4, 31
	v_xor_b32_e32 v44, 32, v36
	v_cndmask_b32_e32 v41, v36, v41, vcc
	v_cmp_lt_i32_e32 vcc, v42, v37
	s_lshl_b64 s[4:5], s[4:5], 13
	s_add_u32 s4, s10, s4
	v_cndmask_b32_e32 v42, v36, v42, vcc
	v_cmp_lt_i32_e32 vcc, v43, v37
	s_addc_u32 s5, s11, s5
	s_ashr_i32 s95, s94, 31
	v_cndmask_b32_e32 v43, v36, v43, vcc
	v_cmp_lt_i32_e32 vcc, v44, v37
	s_ashr_i32 s1, s0, 31
	s_ashr_i32 s10, s83, 31
	v_cndmask_b32_e32 v36, v36, v44, vcc
	v_lshlrev_b32_e32 v77, 2, v36
	v_lshl_add_u64 v[36:37], s[4:5], 0, v[34:35]
	s_lshl_b64 s[4:5], s[94:95], 13
	s_add_u32 s0, s0, s83
	s_addc_u32 s1, s1, s10
	s_lshl_b64 s[0:1], s[0:1], 12
	s_add_u32 s0, s88, s0
	v_add_u32_e32 v71, 0, v34
	v_lshlrev_b32_e32 v34, 3, v38
	s_addc_u32 s1, s89, s1
	s_mov_b64 s[6:7], 0x1000
	s_mov_b64 s[8:9], 0xea00800
	v_lshl_add_u64 v[34:35], s[0:1], 0, v[34:35]
	v_lshlrev_b32_e32 v72, 2, v39
	v_lshlrev_b32_e32 v73, 2, v40
	v_lshlrev_b32_e32 v74, 2, v41
	v_lshlrev_b32_e32 v75, 2, v42
	v_lshlrev_b32_e32 v76, 2, v43
	v_lshl_add_u64 v[66:67], v[36:37], 0, s[6:7]
	v_lshl_add_u64 v[68:69], v[34:35], 0, s[8:9]
	v_mov_b32_e32 v1, 0x358637bd
	s_mov_b32 s3, 0xf800000
	v_mov_b32_e32 v70, 0x260
	s_lshl_b64 s[6:7], s[94:95], 12
	s_waitcnt vmcnt(7)
	v_mov_b64_e32 v[36:37], v[20:21]
	s_waitcnt vmcnt(6)
	v_mov_b64_e32 v[40:41], v[24:25]
	s_waitcnt vmcnt(5)
	v_mov_b64_e32 v[44:45], v[28:29]
	s_waitcnt vmcnt(4)
	v_mov_b64_e32 v[52:53], v[4:5]
	s_waitcnt vmcnt(3)
	v_mov_b64_e32 v[56:57], v[8:9]
	s_waitcnt vmcnt(2)
	v_mov_b64_e32 v[60:61], v[12:13]
	s_waitcnt vmcnt(1)
	v_mov_b64_e32 v[64:65], v[16:17]
	s_waitcnt vmcnt(0)
	v_mov_b64_e32 v[48:49], v[32:33]
	v_mov_b64_e32 v[34:35], v[18:19]
	v_mov_b64_e32 v[38:39], v[22:23]
	v_mov_b64_e32 v[42:43], v[26:27]
	v_mov_b64_e32 v[50:51], v[2:3]
	v_mov_b64_e32 v[54:55], v[6:7]
	v_mov_b64_e32 v[58:59], v[10:11]
	v_mov_b64_e32 v[62:63], v[14:15]
	v_mov_b64_e32 v[46:47], v[30:31]
	s_branch .LBB0_123

.LBB0_123:
	s_add_i32 s2, s2, s94
	s_cmpk_gt_i32 s2, 0x3fff
	s_cselect_b64 s[8:9], -1, 0
	s_and_b64 vcc, exec, s[8:9]
	s_cbranch_vccnz .LBB0_122
	global_load_dwordx4 v[46:49], v[66:67], off offset:-4096
	global_load_dwordx4 v[42:45], v[66:67], off offset:-3072
	global_load_dwordx4 v[38:41], v[66:67], off offset:-2048
	global_load_dwordx4 v[34:37], v[66:67], off offset:-1024
	global_load_dwordx4 v[62:65], v[66:67], off nt
	global_load_dwordx4 v[58:61], v[66:67], off offset:1024
	global_load_dwordx4 v[54:57], v[66:67], off offset:2048
	global_load_dwordx4 v[50:53], v[66:67], off offset:3072
	s_branch .LBB0_122
